# v12_b64exch
# baseline (speedup 1.0000x reference)
.LBB1_50:
	s_or_b64 exec, exec, s[0:1]
	v_and_b32_e32 v1, 31, v0
	v_lshrrev_b32_e32 v24, 8, v0
	v_mad_u32_u24 v19, v24, 42, v1
	v_min_u32_e32 v20, 0x53, v19
	v_lshrrev_b32_e32 v18, 5, v193
	s_movk_i32 s64, 0x110
	v_mul_u32_u24_e32 v25, 0x110, v20
	v_min_u32_e32 v20, 62, v19
	v_lshlrev_b32_e32 v206, 6, v189
	v_mov_b32_e32 v66, 0
	v_mul_u32_u24_e32 v26, 0x110, v20
	v_lshlrev_b32_e32 v204, 4, v18
	v_mad_u32_u24 v22, v19, s64, v206
	v_lshlrev_b32_e32 v27, 3, v18
	v_lshlrev_b32_e32 v18, 1, v183
	v_mov_b32_e32 v19, v66
	v_lshlrev_b32_e32 v20, 10, v185
	v_lshl_add_u64 v[18:19], s[30:31], 0, v[18:19]
	v_and_b32_e32 v20, 0x1000, v20
	v_mov_b32_e32 v21, v66
	v_lshl_add_u64 v[18:19], v[18:19], 0, v[20:21]
	v_mov_b32_e32 v183, v66
	v_lshl_add_u64 v[18:19], v[18:19], 0, v[182:183]
	s_mov_b64 s[6:7], 0x48000
	v_lshl_add_u64 v[208:209], v[18:19], 0, s[6:7]
	v_lshrrev_b32_e32 v18, 2, v0
	v_and_b32_e32 v29, 8, v18
	v_mul_u32_u24_e32 v18, 0x3000, v189
	v_lshlrev_b32_e32 v210, 2, v193
	v_or_b32_e32 v18, v18, v210
	v_add_u32_e32 v221, 0x15a80, v18
	v_add_u32_e32 v221, v221, v210
	v_lshlrev_b32_e32 v18, 6, v193
	v_and_b32_e32 v20, 0xe00, v18
	s_add_u32 s34, s18, 0xc000
	s_movk_i32 s3, 0xff
	v_add_u32_e32 v19, 0x25a80, v210
	v_and_b32_e32 v224, 0x800, v18
	v_or_b32_e32 v225, 0x6600, v20
	v_or_b32_e32 v226, 0x7600, v20
	v_or_b32_e32 v227, 0x8600, v20
	v_or_b32_e32 v228, 0x9600, v20
	v_or_b32_e32 v229, 0x600, v20
	v_or_b32_e32 v230, 0x1600, v20
	v_or_b32_e32 v231, 0x2600, v20
	v_or_b32_e32 v232, 0x3600, v20
	v_or_b32_e32 v233, 0x4600, v20
	v_or_b32_e32 v234, 0x5600, v20
	v_lshlrev_b32_e32 v18, 8, v189
	v_lshlrev_b32_e32 v20, 2, v0
	s_addc_u32 s35, s19, 0
	v_cmp_lt_u32_e64 s[6:7], s3, v0
	v_and_b32_e32 v32, 0x7c, v20
	s_lshl_b32 s3, s2, 3
	v_add_u32_e32 v236, v19, v18
	s_lshl_b32 s2, s2, 5
	v_lshlrev_b32_e32 v18, 14, v185
	v_mov_b32_e32 v19, v66
	v_lshlrev_b32_e32 v20, 15, v189
	v_add_u32_e32 v28, 0x10140, v22
	v_add_u32_e32 v30, 0x11790, v22
	s_and_b32 s67, s3, 0x700
	s_and_b32 s2, s2, 0x1f00
	v_lshl_add_u64 v[18:19], s[30:31], 0, v[18:19]
	v_lshl_add_u64 v[20:21], s[30:31], 0, v[20:21]
	v_lshlrev_b32_e32 v22, 14, v24
	v_mov_b32_e32 v23, v66
	s_add_u32 s38, s34, s2
	v_lshl_add_u64 v[18:19], v[18:19], 0, v[182:183]
	s_mov_b64 s[2:3], 0x60000
	v_lshl_add_u64 v[20:21], v[20:21], 0, v[22:23]
	v_or_b32_e32 v220, v212, v1
	v_lshl_add_u64 v[212:213], v[18:19], 0, s[2:3]
	v_lshl_add_u64 v[20:21], v[20:21], 0, v[182:183]
	s_mov_b64 s[2:3], 0xc0000
	v_lshlrev_b32_e32 v33, 7, v185
	v_lshl_add_u64 v[214:215], v[20:21], 0, s[2:3]
	v_or_b32_e32 v23, 64, v1
	s_movk_i32 s69, 0x410
	v_mov_b32_e32 v20, 0x10140
	v_or_b32_e32 v237, v33, v32
	v_and_b32_e32 v18, 0x1c0, v0
	v_or_b32_e32 v22, v27, v33
	v_mad_u32_u24 v33, v23, s69, v20
	v_lshlrev_b32_e32 v20, 2, v32
	v_mov_b32_e32 v21, v66
	v_or_b32_e32 v31, 0x10140, v204
	v_lshlrev_b32_e32 v18, 2, v18
	v_mov_b32_e32 v19, v66
	s_movk_i32 s68, 0x54
	v_lshl_add_u64 v[216:217], s[26:27], 0, v[20:21]
	v_or_b32_e32 v20, 32, v1
	v_min_i32_e32 v21, 0x53, v23
	s_mov_b32 s37, 0
	v_lshl_or_b32 v207, v24, 7, v31
	v_cmp_eq_u32_e64 s[8:9], 1, v24
	v_lshlrev_b32_e32 v222, 2, v220
	v_lshl_add_u64 v[18:19], s[16:17], 0, v[18:19]
	v_cmp_gt_u32_e64 s[12:13], s68, v23
	v_lshl_or_b32 v24, v24, 9, v31
	v_mul_u32_u24_e32 v20, 0x110, v20
	v_mul_u32_u24_e32 v23, 0x110, v21
	v_mul_u32_u24_e32 v31, 0x410, v1
	v_mul_u32_u24_e32 v21, 0x410, v21
	v_mov_b32_e32 v205, v66
	s_mov_b32 s16, 0x18618618
	v_cmp_gt_u32_e64 s[0:1], 32, v193
	v_cmp_lt_u32_e64 s[14:15], 31, v193
	v_cmp_gt_u32_e64 s[4:5], 21, v1
	s_movk_i32 s65, 0x1000
	s_movk_i32 s66, 0x3000
	v_add_u32_e32 v223, 0x25680, v222
	v_lshl_or_b32 v235, v189, 7, v32
	v_cmp_eq_u32_e64 s[10:11], 0, v193
	s_addc_u32 s39, s35, 0
	v_mul_u32_u24_e32 v238, 0x110, v1
	v_add_u32_e32 v239, 0x10140, v22
	s_add_i32 s70, s33, 16
	s_add_i32 s71, s33, 32
	s_add_i32 s72, s33, 48
	s_add_i32 s73, s33, 64
	s_add_i32 s74, s33, 0x50
	v_lshl_add_u64 v[218:219], v[18:19], 0, v[204:205]
	v_add_u32_e32 v205, v25, v184
	v_add_u32_e32 v240, v26, v204
	v_add_u32_e32 v241, v207, v20
	v_add_u32_e32 v242, v207, v23
	s_movk_i32 s75, 0x2000
	s_movk_i32 s76, 0x100
	s_movk_i32 s77, 0xffc0
	s_mov_b32 s17, 0x3f086186
	s_mov_b32 s78, 0xf800000
	v_mov_b32_e32 v243, 0x260
	s_movk_i32 s79, 0x44
	v_add_u32_e32 v244, v33, v22
	v_add_u32_e32 v245, v24, v31
	v_add_u32_e32 v246, v24, v21
	v_add_u32_e32 v247, v28, v27
	v_add_u32_e32 v248, v30, v29
	v_mov_b32_e32 v249, 0x25680
	s_mov_b32 s36, s37
	s_cmp_eq_u64 s[6:7], 0
	s_cbranch_scc0 .Lprio_skip
	s_setprio 1

.LBB1_61:
	s_or_b64 exec, exec, s[2:3]
	s_nop 8
	v_add_u32_e32 v6, v207, v238
	s_waitcnt lgkmcnt(0)
	s_barrier
	ds_read_b128 v[2:5], v6
	ds_read_b128 v[62:65], v6 offset:32
	ds_read_b128 v[68:71], v6 offset:64
	ds_read_b128 v[72:75], v6 offset:96
	ds_read_b128 v[6:9], v241
	ds_read_b128 v[76:79], v241 offset:32
	ds_read_b128 v[80:83], v241 offset:64
	ds_read_b128 v[84:87], v241 offset:96
	ds_read_b128 v[18:21], v242
	ds_read_b128 v[88:91], v242 offset:32
	ds_read_b128 v[92:95], v242 offset:64
	ds_read_b128 v[96:99], v242 offset:96
	s_waitcnt vmcnt(3) lgkmcnt(11)
	v_mfma_f32_32x32x16_f16 v[34:49], v[2:5], v[100:103], 0
	s_waitcnt lgkmcnt(7)
	v_mfma_f32_32x32x16_f16 v[2:17], v[6:9], v[100:103], 0
	s_waitcnt lgkmcnt(3)
	v_mfma_f32_32x32x16_f16 v[18:33], v[18:21], v[100:103], 0
	s_waitcnt vmcnt(2)
	v_mfma_f32_32x32x16_f16 v[34:49], v[62:65], v[58:61], v[34:49]
	v_mfma_f32_32x32x16_f16 v[2:17], v[76:79], v[58:61], v[2:17]
	s_waitcnt lgkmcnt(2)
	v_mfma_f32_32x32x16_f16 v[18:33], v[88:91], v[58:61], v[18:33]
	s_waitcnt vmcnt(1)
	v_mfma_f32_32x32x16_f16 v[34:49], v[68:71], v[54:57], v[34:49]
	v_mfma_f32_32x32x16_f16 v[2:17], v[80:83], v[54:57], v[2:17]
	s_waitcnt lgkmcnt(1)
	v_mfma_f32_32x32x16_f16 v[18:33], v[92:95], v[54:57], v[18:33]
	s_waitcnt vmcnt(0)
	v_mfma_f32_32x32x16_f16 v[34:49], v[72:75], v[50:53], v[34:49]
	v_mfma_f32_32x32x16_f16 v[2:17], v[84:87], v[50:53], v[2:17]
	s_waitcnt lgkmcnt(0)
	v_mfma_f32_32x32x16_f16 v[18:33], v[96:99], v[50:53], v[18:33]
	s_and_saveexec_b64 s[2:3], s[6:7]
	s_xor_b64 s[2:3], exec, s[2:3]
	s_cbranch_execz .LBB1_63
	s_nop 5
	ds_write_b64 v221, v[34:35]
	ds_write_b64 v221, v[36:37] offset:512
	ds_write_b64 v221, v[38:39] offset:1024
	ds_write_b64 v221, v[40:41] offset:1536
	ds_write_b64 v221, v[42:43] offset:2048
	ds_write_b64 v221, v[44:45] offset:2560
	ds_write_b64 v221, v[46:47] offset:3072
	ds_write_b64 v221, v[48:49] offset:3584
	ds_write_b64 v221, v[2:3] offset:4096
	ds_write_b64 v221, v[4:5] offset:4608
	ds_write_b64 v221, v[6:7] offset:5120
	ds_write_b64 v221, v[8:9] offset:5632
.LBB1_63:
	s_andn2_saveexec_b64 s[2:3], s[2:3]
	s_cbranch_execz .LBB1_65
	s_nop 4
	ds_write_b64 v221, v[10:11] offset:6144
	ds_write_b64 v221, v[12:13] offset:6656
	ds_write_b64 v221, v[14:15] offset:7168
	ds_write_b64 v221, v[16:17] offset:7680
	ds_write_b64 v221, v[18:19] offset:8192
	ds_write_b64 v221, v[20:21] offset:8704
	ds_write_b64 v221, v[22:23] offset:9216
	ds_write_b64 v221, v[24:25] offset:9728
	ds_write_b64 v221, v[26:27] offset:10240
	ds_write_b64 v221, v[28:29] offset:10752
.LBB1_65:
	s_or_b64 exec, exec, s[2:3]
	s_waitcnt lgkmcnt(0)
	s_barrier
	ds_read2st64_b32 v[72:73], v223 offset1:2
	v_add_u32_e32 v67, v222, v224
	v_add_u32_e32 v179, v222, v225
	v_add_u32_e32 v178, v222, v226
	v_add_u32_e32 v177, v222, v227
	s_waitcnt lgkmcnt(0)
	v_mov_b32_e32 v30, v73
	v_fma_f32 v32, -v72, v73, 0
	v_add_u32_e32 v176, v222, v228
	s_and_saveexec_b64 s[2:3], s[6:7]
	s_xor_b64 s[2:3], exec, s[2:3]
	s_cbranch_execz .LBB1_75
	ds_read_b64 v[2:3], v221 offset:6144
	ds_read2st64_b32 v[4:5], v67 offset0:96 offset1:98
	ds_read_b64 v[6:7], v221 offset:6656
	ds_read_b64 v[8:9], v221 offset:7168
	ds_read_b64 v[34:35], v221 offset:7680
	s_waitcnt lgkmcnt(4)
	v_pk_add_f32 v[2:3], v[10:11], v[2:3]
	ds_read2st64_b32 v[10:11], v67 offset0:100 offset1:112
	v_pk_add_f32 v[2:3], v[32:33], v[2:3] op_sel_hi:[0,1]
	s_waitcnt lgkmcnt(4)
	v_pk_fma_f32 v[50:51], v[30:31], v[4:5], v[2:3] op_sel_hi:[0,1,1]
	ds_read_b32 v3, v179
	s_waitcnt lgkmcnt(4)
	v_pk_add_f32 v[4:5], v[12:13], v[6:7]
	s_waitcnt lgkmcnt(1)
	v_mov_b32_e32 v2, v10
	v_pk_add_f32 v[4:5], v[32:33], v[4:5] op_sel_hi:[0,1]
	ds_read2st64_b32 v[6:7], v67 offset0:114 offset1:116
	ds_read_b32 v13, v178
	ds_read_b32 v37, v177
	ds_read_b32 v39, v176
	s_waitcnt lgkmcnt(4)
	v_pk_fma_f32 v[52:53], v[30:31], v[2:3], v[4:5] op_sel_hi:[0,1,1]
	v_pk_add_f32 v[2:3], v[14:15], v[8:9]
	v_mov_b32_e32 v4, v11
	v_pk_add_f32 v[2:3], v[32:33], v[2:3] op_sel_hi:[0,1]
	s_waitcnt lgkmcnt(3)
	v_mov_b32_e32 v5, v6
	v_pk_fma_f32 v[54:55], v[30:31], v[4:5], v[2:3] op_sel_hi:[0,1,1]
	v_pk_add_f32 v[2:3], v[16:17], v[34:35]
	v_mov_b32_e32 v12, v7
	v_pk_add_f32 v[2:3], v[32:33], v[2:3] op_sel_hi:[0,1]
	s_waitcnt lgkmcnt(2)
	v_pk_fma_f32 v[56:57], v[30:31], v[12:13], v[2:3] op_sel_hi:[0,1,1]
	ds_read_b64 v[2:3], v221 offset:8192
	ds_read2st64_b32 v[4:5], v67 offset0:128 offset1:130
	ds_read_b64 v[6:7], v221 offset:8704
	ds_read_b64 v[8:9], v221 offset:9216
	ds_read_b64 v[10:11], v221 offset:9728
	s_waitcnt lgkmcnt(4)
	v_pk_add_f32 v[2:3], v[18:19], v[2:3]
	ds_read2st64_b32 v[12:13], v67 offset0:132 offset1:144
	v_pk_add_f32 v[2:3], v[32:33], v[2:3] op_sel_hi:[0,1]
	s_waitcnt lgkmcnt(4)
	v_pk_fma_f32 v[58:59], v[30:31], v[4:5], v[2:3] op_sel_hi:[0,1,1]
	ds_read2st64_b32 v[4:5], v67 offset0:146 offset1:148
	s_waitcnt lgkmcnt(4)
	v_pk_add_f32 v[2:3], v[20:21], v[6:7]
	s_waitcnt lgkmcnt(1)
	v_mov_b32_e32 v36, v12
	v_pk_add_f32 v[2:3], v[32:33], v[2:3] op_sel_hi:[0,1]
	v_pk_fma_f32 v[60:61], v[30:31], v[36:37], v[2:3] op_sel_hi:[0,1,1]
	v_pk_add_f32 v[2:3], v[22:23], v[8:9]
	v_mov_b32_e32 v6, v13
	v_pk_add_f32 v[2:3], v[32:33], v[2:3] op_sel_hi:[0,1]
	s_waitcnt lgkmcnt(0)
	v_mov_b32_e32 v7, v4
	v_pk_fma_f32 v[62:63], v[30:31], v[6:7], v[2:3] op_sel_hi:[0,1,1]
	v_pk_add_f32 v[2:3], v[24:25], v[10:11]
	v_mov_b32_e32 v38, v5
	v_pk_add_f32 v[2:3], v[32:33], v[2:3] op_sel_hi:[0,1]
	v_pk_fma_f32 v[64:65], v[30:31], v[38:39], v[2:3] op_sel_hi:[0,1,1]
	s_and_saveexec_b64 s[26:27], s[14:15]
	s_xor_b64 s[26:27], exec, s[26:27]
	v_mov_b32_e32 v69, v64
	s_or_saveexec_b64 s[26:27], s[26:27]
	v_pk_add_f32 v[2:3], v[50:51], v[50:51] op_sel:[0,1] op_sel_hi:[1,0]
	v_mov_b32_e32 v4, v50
	v_pk_add_f32 v[2:3], v[2:3], v[52:53]
	v_mov_b32_e32 v5, v52
	v_pk_add_f32 v[2:3], v[2:3], v[52:53] op_sel:[0,1] op_sel_hi:[1,0]
	v_pk_mul_f32 v[4:5], v[4:5], v[4:5]
	v_pk_add_f32 v[2:3], v[2:3], v[54:55]
	v_pk_mov_b32 v[6:7], v[52:53], v[54:55] op_sel:[1,0]
	v_pk_add_f32 v[2:3], v[2:3], v[54:55] op_sel:[0,1] op_sel_hi:[1,0]
	v_pk_mul_f32 v[6:7], v[6:7], v[6:7]
	v_pk_add_f32 v[2:3], v[2:3], v[56:57]
	v_pk_mov_b32 v[8:9], v[54:55], v[56:57] op_sel:[1,0]
	v_pk_add_f32 v[2:3], v[2:3], v[56:57] op_sel:[0,1] op_sel_hi:[1,0]
	v_pk_mul_f32 v[8:9], v[8:9], v[8:9]
	v_pk_add_f32 v[2:3], v[2:3], v[58:59]
	v_pk_mov_b32 v[10:11], v[56:57], v[58:59] op_sel:[1,0]
	v_fma_f32 v3, v51, v51, v4
	v_add_f32_e32 v3, v3, v5
	v_add_f32_e32 v3, v3, v6
	v_add_f32_e32 v3, v3, v7
	v_add_f32_e32 v3, v3, v8
	v_add_f32_e32 v4, v3, v9
	v_fmac_f32_e32 v4, v57, v57
	v_pk_fma_f32 v[4:5], v[10:11], v[10:11], v[4:5] op_sel_hi:[1,1,0]
	v_pk_mul_f32 v[6:7], v[58:59], v[58:59]
	v_mov_b32_e32 v4, v59
	v_mov_b32_e32 v3, v7
	v_pk_add_f32 v[2:3], v[2:3], v[4:5]
	v_pk_mul_f32 v[4:5], v[60:61], v[60:61]
	v_mov_b32_e32 v8, v60
	v_mov_b32_e32 v9, v4
	v_pk_mul_f32 v[6:7], v[62:63], v[62:63]
	v_pk_add_f32 v[2:3], v[2:3], v[8:9]
	v_mov_b32_e32 v4, v61
	v_pk_add_f32 v[2:3], v[2:3], v[4:5]
	v_mov_b32_e32 v4, v62
	v_mov_b32_e32 v5, v6
	v_pk_add_f32 v[2:3], v[2:3], v[4:5]
	v_mov_b32_e32 v6, v63
	v_pk_mul_f32 v[4:5], v[64:65], v[64:65]
	v_pk_add_f32 v[2:3], v[2:3], v[6:7]
	v_mov_b32_e32 v6, v64
	v_mov_b32_e32 v7, v4
	v_pk_add_f32 v[2:3], v[2:3], v[6:7]
	v_mov_b32_e32 v4, v65
	v_mov_b32_e32 v33, v32
	v_mov_b32_e32 v31, v30
	v_pk_add_f32 v[78:79], v[2:3], v[4:5]
	v_mov_b32_e32 v70, 0
	v_mov_b32_e32 v71, 0
	s_xor_b64 exec, exec, s[26:27]
	s_cbranch_execz .LBB1_70
	ds_read_b64 v[2:3], v221 offset:10240
	ds_read2st64_b32 v[4:5], v222 offset0:160 offset1:162
	v_mov_b32_e32 v69, v64
	s_waitcnt lgkmcnt(1)
	v_pk_add_f32 v[2:3], v[26:27], v[2:3]
	s_nop 0
	v_pk_add_f32 v[2:3], v[32:33], v[2:3]
	s_waitcnt lgkmcnt(0)
	v_pk_fma_f32 v[70:71], v[30:31], v[4:5], v[2:3]
	s_nop 0
	v_pk_mul_f32 v[2:3], v[70:71], v[70:71]
	v_mov_b32_e32 v4, v70
	v_mov_b32_e32 v5, v2
	v_mov_b32_e32 v2, v71
	v_pk_add_f32 v[4:5], v[78:79], v[4:5]
	s_nop 0
	v_pk_add_f32 v[78:79], v[4:5], v[2:3]
.LBB1_70:
	s_or_b64 exec, exec, s[26:27]
	s_and_saveexec_b64 s[26:27], s[14:15]
	s_xor_b64 s[26:27], exec, s[26:27]
	s_or_saveexec_b64 s[26:27], s[26:27]
	v_mov_b32_e32 v74, 0
	v_mov_b32_e32 v77, 0
	s_xor_b64 exec, exec, s[26:27]
	s_cbranch_execz .LBB1_74
	ds_read_b64 v[2:3], v221 offset:10752
	ds_read2st64_b32 v[4:5], v222 offset0:164 offset1:166
	s_waitcnt lgkmcnt(1)
	v_pk_add_f32 v[2:3], v[28:29], v[2:3]
	s_nop 0
	v_pk_add_f32 v[2:3], v[32:33], v[2:3]
	s_waitcnt lgkmcnt(0)
	v_pk_fma_f32 v[74:75], v[30:31], v[4:5], v[2:3]
	s_nop 0
	v_pk_mul_f32 v[2:3], v[74:75], v[74:75]
	v_mov_b32_e32 v4, v74
	v_mov_b32_e32 v5, v2
	v_mov_b32_e32 v2, v75
	v_pk_add_f32 v[4:5], v[78:79], v[4:5]
	v_mov_b32_e32 v77, v75
	v_pk_add_f32 v[78:79], v[4:5], v[2:3]

.LBB1_75:
	s_or_saveexec_b64 s[2:3], s[2:3]
	v_mov_b32_e32 v11, 0
	v_add_u32_e32 v251, v222, v229
	v_add_u32_e32 v250, v222, v230
	v_add_u32_e32 v195, v222, v231
	v_add_u32_e32 v194, v222, v232
	v_add_u32_e32 v193, v222, v233
	v_add_u32_e32 v192, v222, v234
	v_mov_b32_e32 v12, 0
	v_mov_b32_e32 v13, 0
	v_mov_b32_e32 v15, 0
	s_xor_b64 exec, exec, s[2:3]
	s_cbranch_execz .LBB1_77
	ds_read_b64 v[10:11], v221
	ds_read2st64_b32 v[12:13], v67 offset1:2
	ds_read_b64 v[14:15], v221 offset:512
	ds_read_b64 v[16:17], v221 offset:1024
	ds_read_b64 v[18:19], v221 offset:1536
	s_waitcnt lgkmcnt(4)
	v_pk_add_f32 v[10:11], v[34:35], v[10:11]
	v_mov_b32_e32 v75, v30
	v_pk_add_f32 v[10:11], v[32:33], v[10:11] op_sel_hi:[0,1]
	s_waitcnt lgkmcnt(3)
	v_pk_fma_f32 v[50:51], v[30:31], v[12:13], v[10:11] op_sel_hi:[0,1,1]
	ds_read2st64_b32 v[12:13], v67 offset0:4 offset1:16
	ds_read_b32 v23, v251
	ds_read_b32 v25, v250
	ds_read_b32 v27, v195
	ds_read_b32 v29, v194
	ds_read_b32 v35, v193
	ds_read_b32 v31, v192
	s_waitcnt lgkmcnt(9)
	v_pk_add_f32 v[14:15], v[36:37], v[14:15]
	v_mul_f32_e32 v20, v51, v51
	v_pk_add_f32 v[14:15], v[32:33], v[14:15] op_sel_hi:[0,1]
	s_waitcnt lgkmcnt(6)
	v_mov_b32_e32 v22, v12
	v_pk_fma_f32 v[20:21], v[50:51], v[50:51], v[20:21] op_sel_hi:[1,1,0]
	s_waitcnt lgkmcnt(0)
	v_pk_fma_f32 v[52:53], v[30:31], v[22:23], v[14:15] op_sel_hi:[0,1,1]
	v_pk_fma_f32 v[14:15], v[52:53], v[52:53], v[20:21]
	ds_read2st64_b32 v[20:21], v67 offset0:18 offset1:20
	v_mul_f32_e32 v12, v53, v53
	v_pk_add_f32 v[16:17], v[38:39], v[16:17]
	v_pk_add_f32 v[14:15], v[14:15], v[12:13] op_sel_hi:[1,0]
	v_pk_add_f32 v[16:17], v[32:33], v[16:17] op_sel_hi:[0,1]
	v_mov_b32_e32 v12, v13
	s_waitcnt lgkmcnt(0)
	v_mov_b32_e32 v13, v20
	v_pk_fma_f32 v[54:55], v[30:31], v[12:13], v[16:17] op_sel_hi:[0,1,1]
	v_pk_fma_f32 v[12:13], v[54:55], v[54:55], v[14:15]
	v_mul_f32_e32 v14, v55, v55
	v_pk_add_f32 v[12:13], v[12:13], v[14:15] op_sel_hi:[1,0]
	v_pk_add_f32 v[14:15], v[40:41], v[18:19]
	v_mov_b32_e32 v24, v21
	v_pk_add_f32 v[14:15], v[32:33], v[14:15] op_sel_hi:[0,1]
	v_pk_fma_f32 v[56:57], v[30:31], v[24:25], v[14:15] op_sel_hi:[0,1,1]
	v_pk_fma_f32 v[12:13], v[56:57], v[56:57], v[12:13]
	v_mul_f32_e32 v14, v57, v57
	v_pk_add_f32 v[12:13], v[12:13], v[14:15] op_sel_hi:[1,0]
	ds_read_b64 v[14:15], v221 offset:2048
	ds_read2st64_b32 v[16:17], v67 offset0:32 offset1:34
	ds_read_b64 v[18:19], v221 offset:2560
	ds_read_b64 v[20:21], v221 offset:3072
	ds_read_b64 v[22:23], v221 offset:3584
	s_waitcnt lgkmcnt(4)
	v_pk_add_f32 v[14:15], v[42:43], v[14:15]
	v_pk_add_f32 v[10:11], v[50:51], v[50:51] op_sel:[0,1] op_sel_hi:[1,0]
	v_pk_add_f32 v[14:15], v[32:33], v[14:15] op_sel_hi:[0,1]
	s_waitcnt lgkmcnt(3)
	v_pk_fma_f32 v[58:59], v[30:31], v[16:17], v[14:15] op_sel_hi:[0,1,1]
	ds_read2st64_b32 v[14:15], v67 offset0:36 offset1:48
	v_pk_add_f32 v[10:11], v[10:11], v[52:53]
	v_pk_fma_f32 v[12:13], v[58:59], v[58:59], v[12:13]
	v_mul_f32_e32 v16, v59, v59
	v_pk_add_f32 v[10:11], v[10:11], v[52:53] op_sel:[0,1] op_sel_hi:[1,0]
	v_pk_add_f32 v[12:13], v[12:13], v[16:17] op_sel_hi:[1,0]
	s_waitcnt lgkmcnt(3)
	v_pk_add_f32 v[16:17], v[44:45], v[18:19]
	v_pk_add_f32 v[10:11], v[10:11], v[54:55]
	v_pk_add_f32 v[16:17], v[32:33], v[16:17] op_sel_hi:[0,1]
	s_waitcnt lgkmcnt(0)
	v_mov_b32_e32 v26, v14
	v_pk_add_f32 v[10:11], v[10:11], v[54:55] op_sel:[0,1] op_sel_hi:[1,0]
	v_pk_fma_f32 v[60:61], v[30:31], v[26:27], v[16:17] op_sel_hi:[0,1,1]
	ds_read2st64_b32 v[16:17], v67 offset0:50 offset1:52
	v_pk_add_f32 v[10:11], v[10:11], v[56:57]
	v_pk_fma_f32 v[12:13], v[60:61], v[60:61], v[12:13]
	v_pk_add_f32 v[10:11], v[10:11], v[56:57] op_sel:[0,1] op_sel_hi:[1,0]
	v_mul_f32_e32 v14, v61, v61
	v_pk_add_f32 v[10:11], v[10:11], v[58:59]
	v_pk_add_f32 v[18:19], v[46:47], v[20:21]
	v_pk_add_f32 v[10:11], v[10:11], v[58:59] op_sel:[0,1] op_sel_hi:[1,0]
	v_pk_add_f32 v[12:13], v[12:13], v[14:15] op_sel_hi:[1,0]
	v_pk_add_f32 v[10:11], v[10:11], v[60:61]
	v_pk_add_f32 v[18:19], v[32:33], v[18:19] op_sel_hi:[0,1]
	v_mov_b32_e32 v14, v15
	s_waitcnt lgkmcnt(0)
	v_mov_b32_e32 v15, v16
	v_pk_fma_f32 v[62:63], v[30:31], v[14:15], v[18:19] op_sel_hi:[0,1,1]
	v_mov_b32_e32 v11, v22
	v_pk_mov_b32 v[18:19], v[60:61], v[48:49] op_sel:[1,0]
	v_pk_mul_f32 v[14:15], v[62:63], v[62:63]
	v_pk_add_f32 v[10:11], v[10:11], v[18:19]
	v_mov_b32_e32 v18, v62
	v_mov_b32_e32 v19, v32
	v_mul_f32_e32 v17, v73, v17
	v_pk_add_f32 v[10:11], v[10:11], v[18:19]
	v_mov_b32_e32 v16, v63
	v_mov_b32_e32 v13, v49
	v_mov_b32_e32 v22, v14
	v_pk_add_f32 v[68:69], v[10:11], v[16:17]
	v_pk_add_f32 v[12:13], v[12:13], v[22:23]
	v_mov_b32_e32 v14, v15
	v_mov_b32_e32 v15, v32
	v_pk_add_f32 v[12:13], v[14:15], v[12:13]
	v_mov_b32_e32 v14, v69
	v_mov_b32_e32 v15, v30
	v_mov_b32_e32 v28, v69
	v_pk_fma_f32 v[64:65], v[14:15], v[28:29], v[12:13]
	ds_read_b64 v[14:15], v221 offset:4096
	ds_read2st64_b32 v[16:17], v67 offset0:64 offset1:66
	ds_read_b64 v[18:19], v221 offset:4608
	ds_read_b64 v[20:21], v221 offset:5120
	ds_read_b64 v[22:23], v221 offset:5632
	s_waitcnt lgkmcnt(4)
	v_pk_add_f32 v[2:3], v[2:3], v[14:15]
	ds_read2st64_b32 v[14:15], v67 offset0:68 offset1:80
	v_pk_add_f32 v[2:3], v[32:33], v[2:3] op_sel_hi:[0,1]
	v_mul_f32_e32 v12, v65, v65
	s_waitcnt lgkmcnt(4)
	v_pk_fma_f32 v[70:71], v[30:31], v[16:17], v[2:3] op_sel_hi:[0,1,1]
	v_pk_add_f32 v[12:13], v[64:65], v[12:13] op_sel_hi:[1,0]
	v_pk_mul_f32 v[2:3], v[70:71], v[70:71]
	s_waitcnt lgkmcnt(3)
	v_add_f32_e32 v4, v4, v18
	v_add_f32_e32 v74, v32, v4
	v_mov_b32_e32 v13, v5
	v_mov_b32_e32 v18, v2
	v_pk_add_f32 v[10:11], v[68:69], v[68:69] op_sel:[0,1] op_sel_hi:[1,0]
	s_waitcnt lgkmcnt(0)
	v_fmac_f32_e32 v74, v73, v14
	v_pk_add_f32 v[4:5], v[12:13], v[18:19]
	v_mov_b32_e32 v2, v3
	v_mov_b32_e32 v3, v32
	ds_read2st64_b32 v[12:13], v67 offset0:82 offset1:84
	v_pk_add_f32 v[10:11], v[10:11], v[64:65] op_sel:[0,1] op_sel_hi:[1,0]
	v_pk_add_f32 v[2:3], v[2:3], v[4:5]
	v_mov_b32_e32 v34, v74
	v_pk_fma_f32 v[76:77], v[74:75], v[34:35], v[2:3]
	v_mul_f32_e32 v75, v73, v15
	v_mov_b32_e32 v11, v6
	v_mov_b32_e32 v4, v70
	v_mov_b32_e32 v5, v20
	v_mov_b32_e32 v6, v7
	v_mov_b32_e32 v7, v8
	v_mov_b32_e32 v14, v21
	v_mov_b32_e32 v15, v22
	v_pk_add_f32 v[4:5], v[10:11], v[4:5]
	v_mov_b32_e32 v10, v71
	v_mov_b32_e32 v11, v32
	v_pk_add_f32 v[6:7], v[6:7], v[14:15]
	v_mul_f32_e32 v2, v77, v77
	v_pk_add_f32 v[4:5], v[10:11], v[4:5]
	v_pk_add_f32 v[6:7], v[32:33], v[6:7] op_sel_hi:[0,1]
	v_pk_add_f32 v[2:3], v[76:77], v[2:3] op_sel_hi:[1,0]
	v_pk_add_f32 v[10:11], v[4:5], v[74:75]
	s_waitcnt lgkmcnt(0)
	v_pk_fma_f32 v[12:13], v[30:31], v[12:13], v[6:7] op_sel_hi:[0,1,1]
	v_pk_add_f32 v[4:5], v[10:11], v[76:77] op_sel:[0,1] op_sel_hi:[1,0]
	v_pk_mul_f32 v[6:7], v[12:13], v[12:13]
	v_mov_b32_e32 v3, v9
	v_mul_f32_e32 v22, v11, v11
	v_pk_add_f32 v[4:5], v[4:5], v[10:11] op_sel:[0,1] op_sel_hi:[1,0]
	v_pk_add_f32 v[2:3], v[2:3], v[22:23]
	v_mov_b32_e32 v7, v32
	v_pk_add_f32 v[4:5], v[4:5], v[12:13]
	v_pk_add_f32 v[2:3], v[6:7], v[2:3]
	v_mov_b32_e32 v6, v13
	v_mov_b32_e32 v7, v30
	v_mov_b32_e32 v30, v13
	v_pk_add_f32 v[4:5], v[4:5], v[12:13] op_sel:[0,1] op_sel_hi:[1,0]
	v_pk_fma_f32 v[14:15], v[6:7], v[30:31], v[2:3]
	s_nop 0
	v_pk_add_f32 v[2:3], v[4:5], v[14:15] op_sel:[0,1] op_sel_hi:[1,0]
	v_mul_f32_e32 v4, v15, v15
	v_pk_add_f32 v[4:5], v[14:15], v[4:5] op_sel_hi:[1,0]
	v_mov_b32_e32 v3, v2
	v_mov_b32_e32 v33, v4
	s_nop 0
	v_permlane32_swap_b32_e32 v2, v3
	v_permlane32_swap_b32_e32 v4, v33
	v_add_f32_e32 v31, v2, v3
	v_mov_b32_e32 v79, v4

.LBB1_142:
	s_or_b64 exec, exec, s[2:3]
	s_nop 8
	v_add_co_u32_e32 v2, vcc, 0x2000, v174
	s_nop 1
	v_addc_co_u32_e32 v3, vcc, 0, v175, vcc
	global_load_dwordx4 v[68:71], v[2:3], off
	global_load_dwordx4 v[72:75], v[2:3], off offset:1024
	global_load_dwordx4 v[84:87], v[2:3], off offset:2048
	global_load_dwordx4 v[88:91], v[2:3], off offset:3072
	v_add_co_u32_e32 v2, vcc, 0x3000, v174
	s_nop 1
	v_addc_co_u32_e32 v3, vcc, 0, v175, vcc
	global_load_dwordx4 v[92:95], v[2:3], off
	global_load_dwordx4 v[96:99], v[2:3], off offset:1024
	global_load_dwordx4 v[100:103], v[2:3], off offset:2048
	global_load_dwordx4 v[104:107], v[2:3], off offset:3072
	s_waitcnt lgkmcnt(0)
	s_barrier
	ds_read_b128 v[2:5], v245 offset:33280
	ds_read_b128 v[108:111], v245 offset:33312
	ds_read_b128 v[18:21], v246
	ds_read_b128 v[112:115], v246 offset:32
	ds_read_b128 v[116:119], v245 offset:32
	ds_read_b128 v[120:123], v245 offset:64
	ds_read_b128 v[6:9], v245
	ds_read_b128 v[124:127], v245 offset:33344
	ds_read_b128 v[128:131], v246 offset:64
	s_waitcnt vmcnt(15) lgkmcnt(2)
	v_mfma_f32_32x32x16_f16 v[34:49], v[6:9], v[136:139], 0
	v_mfma_f32_32x32x16_f16 v[2:17], v[2:5], v[136:139], 0
	v_mfma_f32_32x32x16_f16 v[18:33], v[18:21], v[136:139], 0
	ds_read_b128 v[136:139], v245 offset:96
	ds_read_b128 v[140:143], v245 offset:33376
	ds_read_b128 v[144:147], v246 offset:96
	s_waitcnt vmcnt(14)
	v_mfma_f32_32x32x16_f16 v[34:49], v[116:119], v[132:135], v[34:49]
	v_mfma_f32_32x32x16_f16 v[2:17], v[108:111], v[132:135], v[2:17]
	v_mfma_f32_32x32x16_f16 v[18:33], v[112:115], v[132:135], v[18:33]
	ds_read_b128 v[108:111], v245 offset:128
	ds_read_b128 v[112:115], v245 offset:33408
	ds_read_b128 v[116:119], v246 offset:128
	s_waitcnt vmcnt(13)
	v_mfma_f32_32x32x16_f16 v[34:49], v[120:123], v[80:83], v[34:49]
	s_waitcnt lgkmcnt(7)
	v_mfma_f32_32x32x16_f16 v[2:17], v[124:127], v[80:83], v[2:17]
	s_waitcnt lgkmcnt(6)
	v_mfma_f32_32x32x16_f16 v[18:33], v[128:131], v[80:83], v[18:33]
	ds_read_b128 v[80:83], v245 offset:160
	ds_read_b128 v[120:123], v245 offset:33440
	ds_read_b128 v[124:127], v246 offset:160
	s_waitcnt vmcnt(12) lgkmcnt(8)
	v_mfma_f32_32x32x16_f16 v[34:49], v[136:139], v[76:79], v[34:49]
	s_waitcnt lgkmcnt(7)
	v_mfma_f32_32x32x16_f16 v[2:17], v[140:143], v[76:79], v[2:17]
	s_waitcnt lgkmcnt(6)
	v_mfma_f32_32x32x16_f16 v[18:33], v[144:147], v[76:79], v[18:33]
	ds_read_b128 v[76:79], v245 offset:192
	ds_read_b128 v[128:131], v245 offset:33472
	ds_read_b128 v[132:135], v246 offset:192
	s_waitcnt vmcnt(11) lgkmcnt(8)
	v_mfma_f32_32x32x16_f16 v[34:49], v[108:111], v[62:65], v[34:49]
	s_waitcnt lgkmcnt(7)
	v_mfma_f32_32x32x16_f16 v[2:17], v[112:115], v[62:65], v[2:17]
	s_waitcnt lgkmcnt(6)
	v_mfma_f32_32x32x16_f16 v[18:33], v[116:119], v[62:65], v[18:33]
	ds_read_b128 v[62:65], v245 offset:224
	ds_read_b128 v[108:111], v245 offset:33504
	ds_read_b128 v[112:115], v246 offset:224
	s_waitcnt vmcnt(10) lgkmcnt(8)
	v_mfma_f32_32x32x16_f16 v[34:49], v[80:83], v[58:61], v[34:49]
	s_waitcnt lgkmcnt(7)
	v_mfma_f32_32x32x16_f16 v[2:17], v[120:123], v[58:61], v[2:17]
	s_waitcnt lgkmcnt(6)
	v_mfma_f32_32x32x16_f16 v[18:33], v[124:127], v[58:61], v[18:33]
	ds_read_b128 v[58:61], v245 offset:256
	ds_read_b128 v[80:83], v245 offset:33536
	ds_read_b128 v[116:119], v246 offset:256
	s_waitcnt vmcnt(9) lgkmcnt(8)
	v_mfma_f32_32x32x16_f16 v[34:49], v[76:79], v[54:57], v[34:49]
	s_waitcnt lgkmcnt(7)
	v_mfma_f32_32x32x16_f16 v[2:17], v[128:131], v[54:57], v[2:17]
	s_waitcnt lgkmcnt(6)
	v_mfma_f32_32x32x16_f16 v[18:33], v[132:135], v[54:57], v[18:33]
	ds_read_b128 v[54:57], v245 offset:288
	ds_read_b128 v[76:79], v245 offset:33568
	ds_read_b128 v[120:123], v246 offset:288
	s_waitcnt vmcnt(8) lgkmcnt(8)
	v_mfma_f32_32x32x16_f16 v[34:49], v[62:65], v[50:53], v[34:49]
	s_waitcnt lgkmcnt(7)
	v_mfma_f32_32x32x16_f16 v[2:17], v[108:111], v[50:53], v[2:17]
	s_waitcnt lgkmcnt(6)
	v_mfma_f32_32x32x16_f16 v[18:33], v[112:115], v[50:53], v[18:33]
	ds_read_b128 v[50:53], v245 offset:320
	ds_read_b128 v[62:65], v245 offset:33600
	ds_read_b128 v[108:111], v246 offset:320
	s_waitcnt vmcnt(7) lgkmcnt(8)
	v_mfma_f32_32x32x16_f16 v[34:49], v[58:61], v[68:71], v[34:49]
	s_waitcnt lgkmcnt(7)
	v_mfma_f32_32x32x16_f16 v[2:17], v[80:83], v[68:71], v[2:17]
	s_waitcnt lgkmcnt(6)
	v_mfma_f32_32x32x16_f16 v[18:33], v[116:119], v[68:71], v[18:33]
	ds_read_b128 v[58:61], v245 offset:352
	ds_read_b128 v[68:71], v245 offset:33632
	ds_read_b128 v[80:83], v246 offset:352
	s_waitcnt vmcnt(6) lgkmcnt(8)
	v_mfma_f32_32x32x16_f16 v[34:49], v[54:57], v[72:75], v[34:49]
	s_waitcnt lgkmcnt(7)
	v_mfma_f32_32x32x16_f16 v[2:17], v[76:79], v[72:75], v[2:17]
	s_waitcnt lgkmcnt(6)
	v_mfma_f32_32x32x16_f16 v[18:33], v[120:123], v[72:75], v[18:33]
	ds_read_b128 v[54:57], v245 offset:384
	ds_read_b128 v[72:75], v245 offset:33664
	ds_read_b128 v[76:79], v246 offset:384
	s_waitcnt vmcnt(5) lgkmcnt(8)
	v_mfma_f32_32x32x16_f16 v[34:49], v[50:53], v[84:87], v[34:49]
	s_waitcnt lgkmcnt(7)
	v_mfma_f32_32x32x16_f16 v[2:17], v[62:65], v[84:87], v[2:17]
	s_waitcnt lgkmcnt(6)
	v_mfma_f32_32x32x16_f16 v[18:33], v[108:111], v[84:87], v[18:33]
	ds_read_b128 v[50:53], v245 offset:416
	ds_read_b128 v[62:65], v245 offset:33696
	ds_read_b128 v[84:87], v246 offset:416
	s_waitcnt vmcnt(4) lgkmcnt(8)
	v_mfma_f32_32x32x16_f16 v[34:49], v[58:61], v[88:91], v[34:49]
	s_waitcnt lgkmcnt(7)
	v_mfma_f32_32x32x16_f16 v[2:17], v[68:71], v[88:91], v[2:17]
	s_waitcnt lgkmcnt(6)
	v_mfma_f32_32x32x16_f16 v[18:33], v[80:83], v[88:91], v[18:33]
	ds_read_b128 v[58:61], v245 offset:448
	ds_read_b128 v[68:71], v245 offset:33728
	ds_read_b128 v[80:83], v246 offset:448
	s_waitcnt vmcnt(3) lgkmcnt(8)
	v_mfma_f32_32x32x16_f16 v[34:49], v[54:57], v[92:95], v[34:49]
	s_waitcnt lgkmcnt(7)
	v_mfma_f32_32x32x16_f16 v[2:17], v[72:75], v[92:95], v[2:17]
	s_waitcnt lgkmcnt(6)
	v_mfma_f32_32x32x16_f16 v[18:33], v[76:79], v[92:95], v[18:33]
	ds_read_b128 v[54:57], v245 offset:480
	ds_read_b128 v[72:75], v245 offset:33760
	ds_read_b128 v[76:79], v246 offset:480
	s_waitcnt vmcnt(2) lgkmcnt(8)
	v_mfma_f32_32x32x16_f16 v[34:49], v[50:53], v[96:99], v[34:49]
	s_waitcnt lgkmcnt(7)
	v_mfma_f32_32x32x16_f16 v[2:17], v[62:65], v[96:99], v[2:17]
	s_waitcnt lgkmcnt(6)
	v_mfma_f32_32x32x16_f16 v[18:33], v[84:87], v[96:99], v[18:33]
	s_waitcnt vmcnt(1) lgkmcnt(5)
	v_mfma_f32_32x32x16_f16 v[34:49], v[58:61], v[100:103], v[34:49]
	s_waitcnt lgkmcnt(4)
	v_mfma_f32_32x32x16_f16 v[2:17], v[68:71], v[100:103], v[2:17]
	s_waitcnt lgkmcnt(3)
	v_mfma_f32_32x32x16_f16 v[18:33], v[80:83], v[100:103], v[18:33]
	s_waitcnt vmcnt(0) lgkmcnt(2)
	v_mfma_f32_32x32x16_f16 v[34:49], v[54:57], v[104:107], v[34:49]
	s_waitcnt lgkmcnt(1)
	v_mfma_f32_32x32x16_f16 v[2:17], v[72:75], v[104:107], v[2:17]
	s_waitcnt lgkmcnt(0)
	v_mfma_f32_32x32x16_f16 v[18:33], v[76:79], v[104:107], v[18:33]
	s_barrier
	s_and_saveexec_b64 s[2:3], s[6:7]
	s_xor_b64 s[2:3], exec, s[2:3]
	s_cbranch_execz .LBB1_144
	s_nop 3
	ds_write_b64 v221, v[34:35]
	ds_write_b64 v221, v[36:37] offset:512
	ds_write_b64 v221, v[38:39] offset:1024
	ds_write_b64 v221, v[40:41] offset:1536
	ds_write_b64 v221, v[42:43] offset:2048
	ds_write_b64 v221, v[44:45] offset:2560
	ds_write_b64 v221, v[46:47] offset:3072
	ds_write_b64 v221, v[48:49] offset:3584
	ds_write_b64 v221, v[2:3] offset:4096
	ds_write_b64 v221, v[4:5] offset:4608
	ds_write_b64 v221, v[6:7] offset:5120
	ds_write_b64 v221, v[8:9] offset:5632
.LBB1_144:
	s_andn2_saveexec_b64 s[2:3], s[2:3]
	s_cbranch_execz .LBB1_146
	s_nop 3
	ds_write_b64 v221, v[10:11] offset:6144
	ds_write_b64 v221, v[12:13] offset:6656
	ds_write_b64 v221, v[14:15] offset:7168
	ds_write_b64 v221, v[16:17] offset:7680
	ds_write_b64 v221, v[18:19] offset:8192
	ds_write_b64 v221, v[20:21] offset:8704
	ds_write_b64 v221, v[22:23] offset:9216
	ds_write_b64 v221, v[24:25] offset:9728
	ds_write_b64 v221, v[26:27] offset:10240
	ds_write_b64 v221, v[28:29] offset:10752
.LBB1_146:
	s_or_b64 exec, exec, s[2:3]
	s_waitcnt lgkmcnt(0)
	s_barrier
	ds_read2st64_b32 v[72:73], v223 offset1:2
	s_waitcnt lgkmcnt(0)
	s_nop 0
	v_mov_b32_e32 v30, v73
	v_fma_f32 v32, -v72, v73, v173
	s_and_saveexec_b64 s[2:3], s[6:7]
	s_xor_b64 s[2:3], exec, s[2:3]
	s_cbranch_execz .LBB1_156
	ds_read_b64 v[2:3], v221 offset:6144
	ds_read2st64_b32 v[4:5], v67 offset0:96 offset1:98
	ds_read_b64 v[6:7], v221 offset:6656
	ds_read_b64 v[8:9], v221 offset:7168
	ds_read_b64 v[34:35], v221 offset:7680
	s_waitcnt lgkmcnt(4)
	v_pk_add_f32 v[2:3], v[10:11], v[2:3]
	ds_read2st64_b32 v[10:11], v67 offset0:100 offset1:112
	v_pk_add_f32 v[2:3], v[32:33], v[2:3] op_sel_hi:[0,1]
	s_waitcnt lgkmcnt(4)
	v_pk_fma_f32 v[50:51], v[30:31], v[4:5], v[2:3] op_sel_hi:[0,1,1]
	ds_read_b32 v3, v179
	s_waitcnt lgkmcnt(4)
	v_pk_add_f32 v[4:5], v[12:13], v[6:7]
	s_waitcnt lgkmcnt(1)
	v_mov_b32_e32 v2, v10
	v_pk_add_f32 v[4:5], v[32:33], v[4:5] op_sel_hi:[0,1]
	ds_read2st64_b32 v[6:7], v67 offset0:114 offset1:116
	ds_read_b32 v13, v178
	ds_read_b32 v37, v177
	ds_read_b32 v39, v176
	s_waitcnt lgkmcnt(4)
	v_pk_fma_f32 v[52:53], v[30:31], v[2:3], v[4:5] op_sel_hi:[0,1,1]
	v_pk_add_f32 v[2:3], v[14:15], v[8:9]
	v_mov_b32_e32 v4, v11
	v_pk_add_f32 v[2:3], v[32:33], v[2:3] op_sel_hi:[0,1]
	s_waitcnt lgkmcnt(3)
	v_mov_b32_e32 v5, v6
	v_pk_fma_f32 v[54:55], v[30:31], v[4:5], v[2:3] op_sel_hi:[0,1,1]
	v_pk_add_f32 v[2:3], v[16:17], v[34:35]
	v_mov_b32_e32 v12, v7
	v_pk_add_f32 v[2:3], v[32:33], v[2:3] op_sel_hi:[0,1]
	s_waitcnt lgkmcnt(2)
	v_pk_fma_f32 v[56:57], v[30:31], v[12:13], v[2:3] op_sel_hi:[0,1,1]
	ds_read_b64 v[2:3], v221 offset:8192
	ds_read2st64_b32 v[4:5], v67 offset0:128 offset1:130
	ds_read_b64 v[6:7], v221 offset:8704
	ds_read_b64 v[8:9], v221 offset:9216
	ds_read_b64 v[10:11], v221 offset:9728
	s_waitcnt lgkmcnt(4)
	v_pk_add_f32 v[2:3], v[18:19], v[2:3]
	ds_read2st64_b32 v[12:13], v67 offset0:132 offset1:144
	v_pk_add_f32 v[2:3], v[32:33], v[2:3] op_sel_hi:[0,1]
	s_waitcnt lgkmcnt(4)
	v_pk_fma_f32 v[58:59], v[30:31], v[4:5], v[2:3] op_sel_hi:[0,1,1]
	ds_read2st64_b32 v[4:5], v67 offset0:146 offset1:148
	s_waitcnt lgkmcnt(4)
	v_pk_add_f32 v[2:3], v[20:21], v[6:7]
	s_waitcnt lgkmcnt(1)
	v_mov_b32_e32 v36, v12
	v_pk_add_f32 v[2:3], v[32:33], v[2:3] op_sel_hi:[0,1]
	v_pk_fma_f32 v[60:61], v[30:31], v[36:37], v[2:3] op_sel_hi:[0,1,1]
	v_pk_add_f32 v[2:3], v[22:23], v[8:9]
	v_mov_b32_e32 v6, v13
	v_pk_add_f32 v[2:3], v[32:33], v[2:3] op_sel_hi:[0,1]
	s_waitcnt lgkmcnt(0)
	v_mov_b32_e32 v7, v4
	v_pk_fma_f32 v[62:63], v[30:31], v[6:7], v[2:3] op_sel_hi:[0,1,1]
	v_pk_add_f32 v[2:3], v[24:25], v[10:11]
	v_mov_b32_e32 v38, v5
	v_pk_add_f32 v[2:3], v[32:33], v[2:3] op_sel_hi:[0,1]
	v_pk_fma_f32 v[64:65], v[30:31], v[38:39], v[2:3] op_sel_hi:[0,1,1]
	s_and_saveexec_b64 s[30:31], s[14:15]
	s_xor_b64 s[30:31], exec, s[30:31]
	v_mov_b32_e32 v69, v64
	s_or_saveexec_b64 s[30:31], s[30:31]
	v_add_f32_e32 v2, 0, v50
	v_add_f32_e32 v2, v2, v51
	v_add_f32_e32 v4, v2, v52
	v_mov_b32_e32 v2, v50
	v_mov_b32_e32 v3, v52
	v_pk_mul_f32 v[2:3], v[2:3], v[2:3]
	v_add_f32_e32 v4, v4, v53
	v_add_f32_e32 v6, v4, v54
	v_pk_mov_b32 v[4:5], v[52:53], v[54:55] op_sel:[1,0]
	v_fma_f32 v2, v51, v51, v2
	v_pk_mul_f32 v[4:5], v[4:5], v[4:5]
	v_add_f32_e32 v6, v6, v55
	v_add_f32_e32 v2, v2, v3
	v_add_f32_e32 v8, v6, v56
	v_pk_mov_b32 v[6:7], v[54:55], v[56:57] op_sel:[1,0]
	v_add_f32_e32 v2, v2, v4
	v_pk_mul_f32 v[6:7], v[6:7], v[6:7]
	v_add_f32_e32 v2, v2, v5
	v_add_f32_e32 v2, v2, v6
	v_add_f32_e32 v2, v2, v7
	v_pk_mov_b32 v[10:11], v[56:57], v[58:59] op_sel:[1,0]
	v_fmac_f32_e32 v2, v57, v57
	v_add_f32_e32 v8, v8, v57
	v_pk_fma_f32 v[2:3], v[10:11], v[10:11], v[2:3] op_sel_hi:[1,1,0]
	v_pk_mul_f32 v[4:5], v[58:59], v[58:59]
	v_add_f32_e32 v8, v8, v58
	v_mov_b32_e32 v9, v5
	v_mov_b32_e32 v2, v59
	v_pk_mul_f32 v[4:5], v[60:61], v[60:61]
	v_pk_add_f32 v[2:3], v[8:9], v[2:3]
	v_mov_b32_e32 v8, v60
	v_mov_b32_e32 v9, v4
	v_pk_mul_f32 v[6:7], v[62:63], v[62:63]
	v_pk_add_f32 v[2:3], v[2:3], v[8:9]
	v_mov_b32_e32 v4, v61
	v_pk_add_f32 v[2:3], v[2:3], v[4:5]
	v_mov_b32_e32 v4, v62
	v_mov_b32_e32 v5, v6
	v_pk_add_f32 v[2:3], v[2:3], v[4:5]
	v_mov_b32_e32 v6, v63
	v_pk_mul_f32 v[4:5], v[64:65], v[64:65]
	v_pk_add_f32 v[2:3], v[2:3], v[6:7]
	v_mov_b32_e32 v6, v64
	v_mov_b32_e32 v7, v4
	v_pk_add_f32 v[2:3], v[2:3], v[6:7]
	v_mov_b32_e32 v4, v65
	v_mov_b32_e32 v33, v32
	v_mov_b32_e32 v31, v30
	v_pk_add_f32 v[78:79], v[2:3], v[4:5]
	v_mov_b32_e32 v70, 0
	v_mov_b32_e32 v71, 0
	s_xor_b64 exec, exec, s[30:31]
	s_cbranch_execz .LBB1_151
	ds_read_b64 v[2:3], v221 offset:10240
	ds_read2st64_b32 v[4:5], v222 offset0:160 offset1:162
	v_mov_b32_e32 v69, v64
	s_waitcnt lgkmcnt(1)
	v_pk_add_f32 v[2:3], v[26:27], v[2:3]
	s_nop 0
	v_pk_add_f32 v[2:3], v[32:33], v[2:3]
	s_waitcnt lgkmcnt(0)
	v_pk_fma_f32 v[70:71], v[30:31], v[4:5], v[2:3]
	s_nop 0
	v_pk_mul_f32 v[2:3], v[70:71], v[70:71]
	v_mov_b32_e32 v4, v70
	v_mov_b32_e32 v5, v2
	v_mov_b32_e32 v2, v71
	v_pk_add_f32 v[4:5], v[78:79], v[4:5]
	s_nop 0
	v_pk_add_f32 v[78:79], v[4:5], v[2:3]
.LBB1_151:
	s_or_b64 exec, exec, s[30:31]
	s_and_saveexec_b64 s[30:31], s[14:15]
	s_xor_b64 s[30:31], exec, s[30:31]
	s_or_saveexec_b64 s[30:31], s[30:31]
	v_mov_b32_e32 v74, 0
	v_mov_b32_e32 v77, 0
	s_xor_b64 exec, exec, s[30:31]
	s_cbranch_execz .LBB1_155
	ds_read_b64 v[2:3], v221 offset:10752
	ds_read2st64_b32 v[4:5], v222 offset0:164 offset1:166
	s_waitcnt lgkmcnt(1)
	v_pk_add_f32 v[2:3], v[28:29], v[2:3]
	s_nop 0
	v_pk_add_f32 v[2:3], v[32:33], v[2:3]
	s_waitcnt lgkmcnt(0)
	v_pk_fma_f32 v[74:75], v[30:31], v[4:5], v[2:3]
	s_nop 0
	v_pk_mul_f32 v[2:3], v[74:75], v[74:75]
	v_mov_b32_e32 v4, v74
	v_mov_b32_e32 v5, v2
	v_mov_b32_e32 v2, v75
	v_pk_add_f32 v[4:5], v[78:79], v[4:5]
	v_mov_b32_e32 v77, v75
	v_pk_add_f32 v[78:79], v[4:5], v[2:3]

.LBB1_156:
	s_or_saveexec_b64 s[2:3], s[2:3]
	v_mov_b32_e32 v11, 0
	v_mov_b32_e32 v12, 0
	v_mov_b32_e32 v13, 0
	v_mov_b32_e32 v15, 0
	s_xor_b64 exec, exec, s[2:3]
	s_cbranch_execz .LBB1_158
	ds_read_b64 v[10:11], v221
	ds_read2st64_b32 v[12:13], v67 offset1:2
	ds_read_b64 v[14:15], v221 offset:512
	ds_read_b64 v[16:17], v221 offset:1024
	ds_read_b64 v[18:19], v221 offset:1536
	s_waitcnt lgkmcnt(4)
	v_pk_add_f32 v[10:11], v[34:35], v[10:11]
	v_mov_b32_e32 v75, v30
	v_pk_add_f32 v[10:11], v[32:33], v[10:11] op_sel_hi:[0,1]
	s_waitcnt lgkmcnt(3)
	v_pk_fma_f32 v[50:51], v[30:31], v[12:13], v[10:11] op_sel_hi:[0,1,1]
	v_add_f32_e32 v10, 0, v50
	v_add_f32_e32 v22, v10, v51
	ds_read2st64_b32 v[10:11], v67 offset0:4 offset1:16
	ds_read_b32 v21, v251
	ds_read_b32 v23, v250
	ds_read_b32 v25, v195
	ds_read_b32 v27, v194
	ds_read_b32 v29, v193
	ds_read_b32 v31, v192
	s_waitcnt lgkmcnt(9)
	v_pk_add_f32 v[14:15], v[36:37], v[14:15]
	v_mul_f32_e32 v12, v51, v51
	v_pk_add_f32 v[14:15], v[32:33], v[14:15] op_sel_hi:[0,1]
	s_waitcnt lgkmcnt(6)
	v_mov_b32_e32 v20, v10
	s_waitcnt lgkmcnt(0)
	v_pk_fma_f32 v[52:53], v[30:31], v[20:21], v[14:15] op_sel_hi:[0,1,1]
	ds_read2st64_b32 v[14:15], v67 offset0:18 offset1:20
	v_pk_fma_f32 v[12:13], v[50:51], v[50:51], v[12:13] op_sel_hi:[1,1,0]
	v_add_f32_e32 v10, v22, v52
	v_add_f32_e32 v20, v10, v53
	v_pk_fma_f32 v[12:13], v[52:53], v[52:53], v[12:13]
	v_mul_f32_e32 v10, v53, v53
	v_pk_add_f32 v[16:17], v[38:39], v[16:17]
	v_pk_add_f32 v[12:13], v[12:13], v[10:11] op_sel_hi:[1,0]
	v_pk_add_f32 v[16:17], v[32:33], v[16:17] op_sel_hi:[0,1]
	v_mov_b32_e32 v10, v11
	s_waitcnt lgkmcnt(0)
	v_mov_b32_e32 v11, v14
	v_pk_fma_f32 v[54:55], v[30:31], v[10:11], v[16:17] op_sel_hi:[0,1,1]
	v_add_f32_e32 v10, v20, v54
	v_add_f32_e32 v14, v10, v55
	v_pk_fma_f32 v[10:11], v[54:55], v[54:55], v[12:13]
	v_mul_f32_e32 v12, v55, v55
	v_pk_add_f32 v[10:11], v[10:11], v[12:13] op_sel_hi:[1,0]
	v_pk_add_f32 v[12:13], v[40:41], v[18:19]
	v_mov_b32_e32 v22, v15
	v_pk_add_f32 v[12:13], v[32:33], v[12:13] op_sel_hi:[0,1]
	v_pk_fma_f32 v[56:57], v[30:31], v[22:23], v[12:13] op_sel_hi:[0,1,1]
	v_add_f32_e32 v12, v14, v56
	v_add_f32_e32 v22, v12, v57
	v_pk_fma_f32 v[10:11], v[56:57], v[56:57], v[10:11]
	v_mul_f32_e32 v12, v57, v57
	v_pk_add_f32 v[10:11], v[10:11], v[12:13] op_sel_hi:[1,0]
	ds_read_b64 v[12:13], v221 offset:2048
	ds_read2st64_b32 v[14:15], v67 offset0:32 offset1:34
	ds_read_b64 v[16:17], v221 offset:2560
	ds_read_b64 v[18:19], v221 offset:3072
	ds_read_b64 v[20:21], v221 offset:3584
	s_waitcnt lgkmcnt(4)
	v_pk_add_f32 v[12:13], v[42:43], v[12:13]
	s_nop 0
	v_pk_add_f32 v[12:13], v[32:33], v[12:13] op_sel_hi:[0,1]
	s_waitcnt lgkmcnt(3)
	v_pk_fma_f32 v[58:59], v[30:31], v[14:15], v[12:13] op_sel_hi:[0,1,1]
	v_add_f32_e32 v12, v22, v58
	v_add_f32_e32 v22, v12, v59
	ds_read2st64_b32 v[12:13], v67 offset0:36 offset1:48
	v_pk_fma_f32 v[10:11], v[58:59], v[58:59], v[10:11]
	v_mul_f32_e32 v14, v59, v59
	v_pk_add_f32 v[10:11], v[10:11], v[14:15] op_sel_hi:[1,0]
	s_waitcnt lgkmcnt(3)
	v_pk_add_f32 v[14:15], v[44:45], v[16:17]
	ds_read2st64_b32 v[16:17], v67 offset0:50 offset1:52
	v_pk_add_f32 v[14:15], v[32:33], v[14:15] op_sel_hi:[0,1]
	s_waitcnt lgkmcnt(1)
	v_mov_b32_e32 v24, v12
	v_pk_fma_f32 v[60:61], v[30:31], v[24:25], v[14:15] op_sel_hi:[0,1,1]
	v_pk_fma_f32 v[10:11], v[60:61], v[60:61], v[10:11]
	v_mul_f32_e32 v14, v61, v61
	v_pk_add_f32 v[10:11], v[10:11], v[14:15] op_sel_hi:[1,0]
	v_pk_add_f32 v[14:15], v[46:47], v[18:19]
	v_mov_b32_e32 v18, v13
	v_pk_add_f32 v[14:15], v[32:33], v[14:15] op_sel_hi:[0,1]
	s_waitcnt lgkmcnt(0)
	v_mov_b32_e32 v19, v16
	v_add_f32_e32 v12, v22, v60
	v_pk_fma_f32 v[62:63], v[30:31], v[18:19], v[14:15] op_sel_hi:[0,1,1]
	v_mov_b32_e32 v13, v20
	v_pk_mov_b32 v[18:19], v[60:61], v[48:49] op_sel:[1,0]
	v_pk_mul_f32 v[14:15], v[62:63], v[62:63]
	v_pk_add_f32 v[12:13], v[12:13], v[18:19]
	v_mov_b32_e32 v18, v62
	v_mov_b32_e32 v19, v32
	v_mul_f32_e32 v17, v73, v17
	v_pk_add_f32 v[12:13], v[12:13], v[18:19]
	v_mov_b32_e32 v16, v63
	v_mov_b32_e32 v11, v49
	v_mov_b32_e32 v20, v14
	v_pk_add_f32 v[68:69], v[12:13], v[16:17]
	v_pk_add_f32 v[10:11], v[10:11], v[20:21]
	v_mov_b32_e32 v14, v15
	v_mov_b32_e32 v15, v32
	v_pk_add_f32 v[10:11], v[14:15], v[10:11]
	v_mov_b32_e32 v14, v69
	v_mov_b32_e32 v15, v30
	v_mov_b32_e32 v26, v69
	v_pk_fma_f32 v[64:65], v[14:15], v[26:27], v[10:11]
	ds_read_b64 v[14:15], v221 offset:4096
	ds_read2st64_b32 v[16:17], v67 offset0:64 offset1:66
	ds_read_b64 v[18:19], v221 offset:4608
	ds_read_b64 v[20:21], v221 offset:5120
	ds_read_b64 v[22:23], v221 offset:5632
	s_waitcnt lgkmcnt(4)
	v_pk_add_f32 v[2:3], v[2:3], v[14:15]
	ds_read2st64_b32 v[14:15], v67 offset0:68 offset1:80
	v_pk_add_f32 v[12:13], v[68:69], v[68:69] op_sel:[0,1] op_sel_hi:[1,0]
	v_pk_add_f32 v[2:3], v[32:33], v[2:3] op_sel_hi:[0,1]
	v_pk_add_f32 v[10:11], v[12:13], v[64:65] op_sel:[0,1] op_sel_hi:[1,0]
	v_mul_f32_e32 v12, v65, v65
	s_waitcnt lgkmcnt(4)
	v_pk_fma_f32 v[70:71], v[30:31], v[16:17], v[2:3] op_sel_hi:[0,1,1]
	v_pk_add_f32 v[12:13], v[64:65], v[12:13] op_sel_hi:[1,0]
	v_pk_mul_f32 v[2:3], v[70:71], v[70:71]
	s_waitcnt lgkmcnt(3)
	v_add_f32_e32 v4, v4, v18
	v_add_f32_e32 v74, v32, v4
	v_mov_b32_e32 v13, v5
	v_mov_b32_e32 v18, v2
	s_waitcnt lgkmcnt(0)
	v_fmac_f32_e32 v74, v73, v14
	v_pk_add_f32 v[4:5], v[12:13], v[18:19]
	v_mov_b32_e32 v2, v3
	v_mov_b32_e32 v3, v32
	ds_read2st64_b32 v[12:13], v67 offset0:82 offset1:84
	v_pk_add_f32 v[2:3], v[2:3], v[4:5]
	v_mov_b32_e32 v28, v74
	v_pk_fma_f32 v[76:77], v[74:75], v[28:29], v[2:3]
	v_mul_f32_e32 v75, v73, v15
	v_mov_b32_e32 v11, v6
	v_mov_b32_e32 v4, v70
	v_mov_b32_e32 v5, v20
	v_mov_b32_e32 v6, v7
	v_mov_b32_e32 v7, v8
	v_mov_b32_e32 v14, v21
	v_mov_b32_e32 v15, v22
	v_pk_add_f32 v[4:5], v[10:11], v[4:5]
	v_mov_b32_e32 v10, v71
	v_mov_b32_e32 v11, v32
	v_pk_add_f32 v[6:7], v[6:7], v[14:15]
	v_mul_f32_e32 v2, v77, v77
	v_pk_add_f32 v[4:5], v[10:11], v[4:5]
	v_pk_add_f32 v[6:7], v[32:33], v[6:7] op_sel_hi:[0,1]
	v_pk_add_f32 v[2:3], v[76:77], v[2:3] op_sel_hi:[1,0]
	v_pk_add_f32 v[10:11], v[4:5], v[74:75]
	s_waitcnt lgkmcnt(0)
	v_pk_fma_f32 v[12:13], v[30:31], v[12:13], v[6:7] op_sel_hi:[0,1,1]
	v_pk_add_f32 v[4:5], v[10:11], v[76:77] op_sel:[0,1] op_sel_hi:[1,0]
	v_pk_mul_f32 v[6:7], v[12:13], v[12:13]
	v_mov_b32_e32 v3, v9
	v_mul_f32_e32 v22, v11, v11
	v_pk_add_f32 v[4:5], v[4:5], v[10:11] op_sel:[0,1] op_sel_hi:[1,0]
	v_pk_add_f32 v[2:3], v[2:3], v[22:23]
	v_mov_b32_e32 v7, v32
	v_pk_add_f32 v[4:5], v[4:5], v[12:13]
	v_pk_add_f32 v[2:3], v[6:7], v[2:3]
	v_mov_b32_e32 v6, v13
	v_mov_b32_e32 v7, v30
	v_mov_b32_e32 v30, v13
	v_pk_add_f32 v[4:5], v[4:5], v[12:13] op_sel:[0,1] op_sel_hi:[1,0]
	v_pk_fma_f32 v[14:15], v[6:7], v[30:31], v[2:3]
	s_nop 0
	v_pk_add_f32 v[2:3], v[4:5], v[14:15] op_sel:[0,1] op_sel_hi:[1,0]
	v_mul_f32_e32 v4, v15, v15
	v_pk_add_f32 v[4:5], v[14:15], v[4:5] op_sel_hi:[1,0]
	v_mov_b32_e32 v3, v2
	v_mov_b32_e32 v33, v4
	s_nop 0
	v_permlane32_swap_b32_e32 v2, v3
	v_permlane32_swap_b32_e32 v4, v33
	v_add_f32_e32 v31, v2, v3
	v_mov_b32_e32 v79, v4
